# grid barrier: non-leader workgroups wait on the top-level generation word instead of their XCD's word (one release hop less)
# speedup vs baseline: 1.0067x; 1.0067x over previous
.LBB0_606:
	s_or_b64 exec, exec, s[4:5]
	s_waitcnt lgkmcnt(1)
	v_max_u32_e32 v5, 1, v2
	v_cvt_f32_u32_e32 v6, v5
	s_waitcnt vmcnt(0)
	v_readfirstlane_b32 s2, v4
	v_rcp_iflag_f32_e32 v6, v6
	s_nop 0
	v_add_u32_e32 v4, s2, v1
	v_sub_u32_e32 v1, 0, v5
	v_mul_f32_e32 v6, 0x4f7ffffe, v6
	v_cvt_u32_f32_e32 v6, v6
	v_mul_lo_u32 v1, v1, v6
	v_mul_hi_u32 v1, v6, v1
	v_add_u32_e32 v1, v6, v1
	v_mul_hi_u32 v1, v4, v1
	v_mul_lo_u32 v6, v1, v5
	v_sub_u32_e32 v6, v4, v6
	v_add_u32_e32 v7, 1, v1
	v_cmp_ge_u32_e32 vcc, v6, v5
	v_add_u32_e32 v4, 1, v4
	s_nop 0
	v_cndmask_b32_e32 v1, v1, v7, vcc
	v_sub_u32_e32 v7, v6, v5
	v_cndmask_b32_e32 v6, v6, v7, vcc
	v_add_u32_e32 v7, 1, v1
	v_cmp_ge_u32_e32 vcc, v6, v5
	s_nop 1
	v_cndmask_b32_e32 v1, v1, v7, vcc
	v_mul_lo_u32 v6, v5, v1
	v_add_u32_e32 v5, v6, v5
	v_cmp_ne_u32_e32 vcc, v4, v5
	s_and_saveexec_b64 s[2:3], vcc
	s_xor_b64 s[2:3], exec, s[2:3]
	s_cbranch_execz .LBB0_630
	v_readlane_b32 s4, v253, 13
	v_readlane_b32 s5, v253, 14
	s_nop 4
	global_load_dword v2, v87, s[4:5] sc1
	s_waitcnt vmcnt(0)
	v_cmp_eq_u32_e32 vcc, v2, v1
	s_and_saveexec_b64 s[4:5], vcc
	s_cbranch_execz .LBB0_629
	s_mov_b32 s16, 1
	s_mov_b64 s[6:7], 0
	s_branch .LBB0_610
